# speedup vs baseline: 1.0057x; 1.0057x over previous
_Z10ode_kernelPKfPKDF16_S2_PfPKi:
	v_lshrrev_b32_e32 v167, 6, v0
	s_lshr_b32 s3, s2, 3
	v_add_u32_e32 v2, s3, v167
	s_load_dwordx4 s[4:7], s[0:1], 0x0
	s_load_dwordx2 s[12:13], s[0:1], 0x10
	v_and_b32_e32 v130, 3, v2
	v_and_b32_e32 v1, 63, v0
	v_readfirstlane_b32 s3, v130
	v_lshlrev_b32_e32 v166, 4, v1
	s_lshl_b32 s11, s3, 14
	v_lshl_or_b32 v2, v130, 17, v166
	v_mov_b32_e32 v3, 0
	s_and_b32 s17, s11, 0xc000
	s_mov_b32 s9, 0
	s_waitcnt lgkmcnt(0)
	v_lshl_add_u64 v[74:75], s[6:7], 0, v[2:3]
	s_lshl_b32 s8, s17, 1
	v_lshl_add_u64 v[46:47], v[74:75], 0, s[8:9]
	s_movk_i32 s15, 0x1000
	v_add_co_u32_e32 v18, vcc, s15, v46
	s_movk_i32 s14, 0x3000
	s_nop 0
	v_addc_co_u32_e32 v19, vcc, 0, v47, vcc
	v_add_co_u32_e32 v20, vcc, s14, v46
	s_lshl_b32 s10, s2, 10
	s_nop 0
	v_addc_co_u32_e32 v21, vcc, 0, v47, vcc
	s_and_b32 s8, s10, 0x3e000
	s_movk_i32 s16, 0x7000
	v_add_co_u32_e32 v48, vcc, s16, v46
	v_lshl_or_b32 v22, v1, 7, s8
	s_add_i32 s8, s11, 0x4000
	v_addc_co_u32_e32 v49, vcc, 0, v47, vcc
	s_movk_i32 s16, 0x5000
	s_and_b32 s8, s8, 0xc000
	v_add_co_u32_e32 v50, vcc, s16, v46
	s_lshl_b32 s8, s8, 1
	global_load_dwordx4 v[34:37], v[18:19], off offset:2048
	global_load_dwordx4 v[14:17], v[20:21], off offset:2048
	global_load_dwordx4 v[6:9], v[20:21], off offset:1024
	global_load_dwordx4 v[2:5], v[18:19], off offset:1024
	global_load_dwordx4 v[42:45], v[18:19], off offset:3072
	global_load_dwordx4 v[38:41], v[20:21], off offset:3072
	v_addc_co_u32_e32 v51, vcc, 0, v47, vcc
	v_lshl_add_u64 v[72:73], v[74:75], 0, s[8:9]
	v_add_co_u32_e32 v106, vcc, s14, v72
	global_load_dwordx4 v[10:13], v[50:51], off offset:1024
	global_load_dwordx4 v[52:55], v[50:51], off offset:2048
	global_load_dwordx4 v[56:59], v[48:49], off offset:2048
	v_addc_co_u32_e32 v107, vcc, 0, v73, vcc
	v_add_co_u32_e32 v108, vcc, s15, v72
	global_load_dwordx4 v[60:63], v[50:51], off offset:3072
	global_load_dwordx4 v[64:67], v[48:49], off offset:3072
	global_load_ushort v198, v22, s[12:13]
	v_addc_co_u32_e32 v109, vcc, 0, v73, vcc
	global_load_dwordx4 v[68:71], v[108:109], off offset:2048
	global_load_dwordx4 v[78:81], v[106:107], off offset:2048
	global_load_dwordx4 v[82:85], v[106:107], off offset:3072
	global_load_dwordx4 v[86:89], v[108:109], off offset:3072
	s_add_i32 s8, s11, 0x6000
	s_movk_i32 s16, 0x2000
	s_and_b32 s8, s8, 0xe000
	v_add_co_u32_e32 v26, vcc, s16, v46
	s_lshl_b32 s8, s8, 1
	s_nop 0
	v_addc_co_u32_e32 v27, vcc, 0, v47, vcc
	v_lshl_add_u64 v[110:111], v[74:75], 0, s[8:9]
	v_add_co_u32_e32 v112, vcc, s14, v110
	global_load_dwordx4 a[0:3], v[46:47], off
	global_load_dwordx4 a[8:11], v[46:47], off offset:1024
	global_load_dwordx4 a[12:15], v[26:27], off offset:1024
	global_load_dwordx4 a[20:23], v[26:27], off offset:2048
	global_load_dwordx4 a[16:19], v[46:47], off offset:2048
	global_load_dwordx4 a[24:27], v[46:47], off offset:3072
	global_load_dwordx4 a[4:7], v[20:21], off offset:-4096
	global_load_dwordx4 v[22:25], v[20:21], off
	global_load_dwordx4 a[28:31], v[26:27], off offset:3072
	s_nop 0
	global_load_dwordx4 v[18:21], v[18:19], off
	v_addc_co_u32_e32 v113, vcc, 0, v111, vcc
	v_add_co_u32_e32 v114, vcc, s15, v110
	v_lshl_or_b32 v199, v167, 15, v166
	s_nop 0
	v_addc_co_u32_e32 v115, vcc, 0, v111, vcc
	global_load_dwordx4 v[26:29], v[114:115], off offset:1024
	global_load_dwordx4 v[90:93], v[114:115], off offset:2048
	global_load_dwordx4 v[30:33], v[112:113], off offset:1024
	global_load_dwordx4 v[94:97], v[112:113], off offset:2048
	global_load_dwordx4 v[98:101], v[114:115], off offset:3072
	global_load_dwordx4 v[102:105], v[112:113], off offset:3072
	s_movk_i32 s8, 0x6000
	s_load_dwordx2 s[6:7], s[0:1], 0x20
	v_lshlrev_b32_e32 v76, 1, v0
	v_and_b32_e32 v200, 7, v0
	v_and_b32_e32 v128, 64, v76
	v_and_b32_e32 v179, 15, v0
	v_bfe_u32 v201, v0, 4, 1
	v_mov_b32_e32 v196, 0x44444444
	global_load_dwordx4 a[44:47], v[48:49], off offset:-4096
	s_waitcnt vmcnt(31)
	ds_write_b128 v199, v[14:17] offset:1024
	v_add_co_u32_e32 v14, vcc, s8, v46
	s_movk_i32 s8, 0x4000
	s_nop 0
	v_addc_co_u32_e32 v15, vcc, 0, v47, vcc
	s_waitcnt vmcnt(28)
	ds_write_b128 v199, v[42:45] offset:2048
	v_add_co_u32_e32 v42, vcc, s8, v46
	ds_write_b128 v199, v[34:37]
	s_nop 0
	v_addc_co_u32_e32 v43, vcc, 0, v47, vcc
	s_waitcnt vmcnt(27)
	ds_write_b128 v199, v[38:41] offset:3072
	v_add_co_u32_e32 v44, vcc, s16, v72
	global_load_dwordx4 a[36:39], v[14:15], off offset:1024
	global_load_dwordx4 a[32:35], v[42:43], off offset:1024
	global_load_dwordx4 a[48:51], v[42:43], off offset:2048
	global_load_dwordx4 a[52:55], v[14:15], off offset:2048
	global_load_dwordx4 a[60:63], v[14:15], off offset:3072
	global_load_dwordx4 a[40:43], v[50:51], off offset:-4096
	global_load_dwordx4 v[34:37], v[50:51], off
	global_load_dwordx4 v[38:41], v[48:49], off
	s_nop 0
	global_load_dwordx4 v[14:17], v[48:49], off offset:1024
	s_waitcnt vmcnt(34)
	ds_write_b128 v199, v[52:55] offset:4096
	s_waitcnt vmcnt(33)
	ds_write_b128 v199, v[56:59] offset:5120
	v_addc_co_u32_e32 v45, vcc, 0, v73, vcc
	s_xor_b32 s8, s17, 0x8000
	global_load_dwordx4 a[68:71], v[106:107], off offset:-4096
	s_waitcnt vmcnt(33)
	ds_write_b128 v199, v[60:63] offset:6144
	s_waitcnt vmcnt(32)
	ds_write_b128 v199, v[64:67] offset:7168
	v_add_co_u32_e32 v58, vcc, s16, v110
	s_lshl_b32 s8, s8, 1
	global_load_dwordx4 a[56:59], v[42:43], off offset:3072
	global_load_dwordx4 a[64:67], v[72:73], off
	global_load_dwordx4 a[72:75], v[72:73], off offset:1024
	global_load_dwordx4 a[80:83], v[72:73], off offset:2048
	global_load_dwordx4 a[84:87], v[44:45], off offset:2048
	global_load_dwordx4 a[92:95], v[44:45], off offset:3072
	global_load_dwordx4 a[76:79], v[44:45], off offset:1024
	global_load_dwordx4 a[88:91], v[72:73], off offset:3072
	global_load_dwordx4 v[46:49], v[106:107], off
	global_load_dwordx4 v[54:57], v[106:107], off offset:1024
	s_nop 0
	global_load_dwordx4 v[42:45], v[108:109], off
	global_load_dwordx4 v[50:53], v[108:109], off offset:1024
	s_waitcnt vmcnt(42)
	ds_write_b128 v199, v[68:71] offset:8192
	s_waitcnt vmcnt(41)
	ds_write_b128 v199, v[78:81] offset:9216
	s_waitcnt vmcnt(39)
	ds_write_b128 v199, v[86:89] offset:10240
	ds_write_b128 v199, v[82:85] offset:11264
	v_addc_co_u32_e32 v59, vcc, 0, v111, vcc
	v_lshl_add_u64 v[78:79], v[74:75], 0, s[8:9]
	v_add_co_u32_e32 v84, vcc, s14, v78
	global_load_dwordx4 a[96:99], v[110:111], off
	global_load_dwordx4 a[104:107], v[110:111], off offset:1024
	global_load_dwordx4 a[108:111], v[58:59], off offset:1024
	global_load_dwordx4 a[116:119], v[58:59], off offset:2048
	global_load_dwordx4 a[112:115], v[110:111], off offset:2048
	global_load_dwordx4 a[120:123], v[110:111], off offset:3072
	global_load_dwordx4 a[100:103], v[112:113], off offset:-4096
	global_load_dwordx4 v[62:65], v[112:113], off
	global_load_dwordx4 a[124:127], v[58:59], off offset:3072
	s_nop 0
	global_load_dwordx4 v[58:61], v[114:115], off
	v_addc_co_u32_e32 v85, vcc, 0, v79, vcc
	v_add_co_u32_e32 v82, vcc, s15, v78
	s_add_i32 s8, s11, 0xa000
	s_nop 0
	v_addc_co_u32_e32 v83, vcc, 0, v79, vcc
	global_load_dwordx4 v[110:113], v[82:83], off offset:2048
	global_load_dwordx4 v[106:109], v[84:85], off offset:2048
	s_waitcnt vmcnt(39)
	ds_write_b128 v199, v[90:93] offset:12288
	s_waitcnt vmcnt(37)
	ds_write_b128 v199, v[94:97] offset:13312
	s_waitcnt vmcnt(36)
	ds_write_b128 v199, v[98:101] offset:14336
	s_waitcnt vmcnt(35)
	ds_write_b128 v199, v[102:105] offset:15360
	global_load_dwordx4 a[128:131], v[78:79], off
	global_load_dwordx4 a[132:135], v[84:85], off offset:-4096
	global_load_dwordx4 a[136:139], v[78:79], off offset:1024
	global_load_dwordx4 a[144:147], v[78:79], off offset:2048
	global_load_dwordx4 v[102:105], v[82:83], off offset:3072
	global_load_dwordx4 v[98:101], v[84:85], off offset:3072
	s_and_b32 s8, s8, 0xe000
	v_add_co_u32_e32 v80, vcc, s16, v78
	s_lshl_b32 s8, s8, 1
	s_nop 0
	v_addc_co_u32_e32 v81, vcc, 0, v79, vcc
	v_lshl_add_u64 v[122:123], v[74:75], 0, s[8:9]
	v_add_co_u32_e32 v124, vcc, s14, v122
	s_add_i32 s8, s11, 0xc000
	s_nop 0
	v_addc_co_u32_e32 v125, vcc, 0, v123, vcc
	v_add_co_u32_e32 v126, vcc, s15, v122
	s_and_b32 s8, s8, 0xc000
	s_nop 0
	v_addc_co_u32_e32 v127, vcc, 0, v123, vcc
	global_load_dwordx4 v[70:73], v[124:125], off offset:1024
	global_load_dwordx4 v[114:117], v[124:125], off offset:2048
	global_load_dwordx4 v[66:69], v[126:127], off offset:1024
	global_load_dwordx4 v[118:121], v[126:127], off offset:2048
	global_load_dwordx4 a[148:151], v[80:81], off offset:2048
	global_load_dwordx4 a[156:159], v[80:81], off offset:3072
	global_load_dwordx4 v[132:135], v[126:127], off offset:3072
	global_load_dwordx4 v[136:139], v[124:125], off offset:3072
	global_load_dwordx4 a[140:143], v[80:81], off offset:1024
	global_load_dwordx4 a[152:155], v[78:79], off offset:3072
	s_nop 0
	global_load_dwordx4 v[78:81], v[84:85], off
	global_load_dwordx4 v[86:89], v[84:85], off offset:1024
	s_lshl_b32 s8, s8, 1
	v_lshl_add_u64 v[164:165], v[74:75], 0, s[8:9]
	v_add_co_u32_e32 v176, vcc, s14, v164
	s_add_i32 s11, s11, 0xe000
	s_nop 0
	v_addc_co_u32_e32 v177, vcc, 0, v165, vcc
	v_add_co_u32_e32 v184, vcc, s15, v164
	s_and_b32 s8, s11, 0xe000
	s_nop 0
	v_addc_co_u32_e32 v185, vcc, 0, v165, vcc
	global_load_dwordx4 v[140:143], v[184:185], off offset:2048
	global_load_dwordx4 v[144:147], v[176:177], off offset:2048
	global_load_dwordx4 v[148:151], v[176:177], off offset:3072
	global_load_dwordx4 v[152:155], v[184:185], off offset:3072
	s_lshl_b32 s8, s8, 1
	v_lshl_add_u64 v[186:187], v[74:75], 0, s[8:9]
	v_add_co_u32_e32 v188, vcc, s14, v186
	v_and_or_b32 v74, v76, 16, v200
	s_nop 0
	v_addc_co_u32_e32 v189, vcc, 0, v187, vcc
	v_add_co_u32_e32 v190, vcc, s15, v186
	v_lshlrev_b32_e32 v129, 2, v74
	s_nop 0
	v_addc_co_u32_e32 v191, vcc, 0, v187, vcc
	global_load_dwordx4 v[94:97], v[188:189], off offset:1024
	global_load_dwordx4 v[156:159], v[188:189], off offset:2048
	global_load_dwordx4 v[90:93], v[190:191], off offset:1024
	global_load_dwordx4 v[160:163], v[190:191], off offset:2048
	global_load_dwordx4 v[172:175], v[188:189], off offset:3072
	global_load_dwordx4 v[180:183], v[190:191], off offset:3072
	s_waitcnt lgkmcnt(0)
	global_load_dword v131, v129, s[6:7]
	global_load_dwordx4 v[74:77], v[82:83], off
	s_nop 0
	global_load_dwordx4 v[82:85], v[82:83], off offset:1024
	s_waitcnt vmcnt(32)
	ds_write_b128 v199, v[110:113] offset:16384
	s_waitcnt vmcnt(31)
	ds_write_b128 v199, v[106:109] offset:17408
	v_lshlrev_b32_e32 v106, 7, v130
	v_or3_b32 v202, v106, v128, v179
	v_lshlrev_b32_e32 v106, 9, v201
	v_or_b32_e32 v107, 32, v129
	v_or3_b32 v106, v106, s10, v202
	global_load_dword v178, v129, s[6:7] offset:128
	global_load_dword v192, v107, s[6:7] offset:128
	global_load_dword v193, v129, s[6:7] offset:32
	v_ashrrev_i32_e32 v107, 31, v106
	v_lshl_add_u64 v[128:129], v[106:107], 2, s[4:5]
	global_load_dword v171, v[128:129], off
	s_waitcnt vmcnt(30)
	ds_write_b128 v199, v[102:105] offset:18432
	s_waitcnt vmcnt(29)
	ds_write_b128 v199, v[98:101] offset:19456
	v_add_co_u32_e32 v98, vcc, s16, v122
	s_mov_b32 s14, 0x45000000
	s_nop 0
	v_addc_co_u32_e32 v99, vcc, 0, v123, vcc
	global_load_dwordx4 a[160:163], v[122:123], off
	global_load_dwordx4 a[168:171], v[122:123], off offset:1024
	global_load_dwordx4 a[172:175], v[98:99], off offset:1024
	global_load_dwordx4 a[180:183], v[98:99], off offset:2048
	global_load_dwordx4 a[176:179], v[122:123], off offset:2048
	global_load_dwordx4 a[184:187], v[122:123], off offset:3072
	global_load_dword v170, v[128:129], off offset:64
	global_load_dwordx4 a[164:167], v[124:125], off offset:-4096
	global_load_dwordx4 v[102:105], v[124:125], off
	global_load_dwordx4 a[188:191], v[98:99], off offset:3072
	s_nop 0
	global_load_dwordx4 v[98:101], v[126:127], off
	s_waitcnt vmcnt(36)
	ds_write_b128 v199, v[118:121] offset:20480
	ds_write_b128 v199, v[114:117] offset:21504
	global_load_dword v169, v[128:129], off offset:128
	v_add_co_u32_e32 v106, vcc, s16, v164
	s_waitcnt vmcnt(34)
	ds_write_b128 v199, v[132:135] offset:22528
	s_waitcnt vmcnt(33)
	ds_write_b128 v199, v[136:139] offset:23552
	v_addc_co_u32_e32 v107, vcc, 0, v165, vcc
	global_load_dwordx4 a[192:195], v[164:165], off
	global_load_dwordx4 a[196:199], v[176:177], off offset:-4096
	global_load_dwordx4 a[200:203], v[164:165], off offset:1024
	global_load_dwordx4 a[208:211], v[164:165], off offset:2048
	global_load_dwordx4 a[212:215], v[106:107], off offset:2048
	global_load_dwordx4 a[220:223], v[106:107], off offset:3072
	global_load_dwordx4 a[204:207], v[106:107], off offset:1024
	global_load_dwordx4 a[216:219], v[164:165], off offset:3072
	global_load_dwordx4 v[110:113], v[176:177], off
	global_load_dwordx4 v[118:121], v[176:177], off offset:1024
	s_nop 0
	global_load_dwordx4 v[106:109], v[184:185], off
	global_load_dwordx4 v[114:117], v[184:185], off offset:1024
	global_load_dword v168, v[128:129], off offset:192
	v_add_co_u32_e32 v122, vcc, s16, v186
	v_and_b32_e32 v133, 32, v0
	s_nop 0
	v_addc_co_u32_e32 v123, vcc, 0, v187, vcc
	s_waitcnt vmcnt(41)
	ds_write_b128 v199, v[140:143] offset:24576
	s_waitcnt vmcnt(40)
	ds_write_b128 v199, v[144:147] offset:25600
	s_waitcnt vmcnt(38)
	ds_write_b128 v199, v[152:155] offset:26624
	ds_write_b128 v199, v[148:151] offset:27648
	global_load_dwordx4 a[224:227], v[186:187], off
	global_load_dwordx4 a[232:235], v[186:187], off offset:1024
	global_load_dwordx4 a[236:239], v[122:123], off offset:1024
	global_load_dwordx4 a[244:247], v[122:123], off offset:2048
	global_load_dwordx4 a[240:243], v[186:187], off offset:2048
	global_load_dwordx4 a[248:251], v[186:187], off offset:3072
	global_load_dwordx4 a[228:231], v[188:189], off offset:-4096
	global_load_dwordx4 v[126:129], v[188:189], off
	global_load_dwordx4 a[252:255], v[122:123], off offset:3072
	s_nop 0
	global_load_dwordx4 v[122:125], v[190:191], off
	v_lshlrev_b32_e32 v132, 2, v201
	v_lshl_or_b32 v130, v130, 6, v133
	v_lshrrev_b32_e32 v139, 1, v0
	v_and_b32_e32 v203, 24, v139
	s_waitcnt vmcnt(44)
	ds_write_b128 v199, v[160:163] offset:28672
	ds_write_b128 v199, v[156:159] offset:29696
	s_waitcnt vmcnt(42)
	ds_write_b128 v199, v[180:183] offset:30720
	ds_write_b128 v199, v[172:175] offset:31744
	s_waitcnt vmcnt(10) lgkmcnt(0)
	v_lshrrev_b32_e32 v222, 2, v131
	v_and_or_b32 v222, v222, 8, v132
	v_mul_u32_u24_e32 v222, 0x110, v222
	v_and_or_b32 v223, v131, 31, v130
	v_add_lshl_u32 v223, v223, v222, 1
	v_or_b32_e32 v204, 0x20000, v223
	v_lshrrev_b32_e32 v222, 2, v178
	v_and_or_b32 v222, v222, 8, v132
	v_mul_u32_u24_e32 v222, 0x110, v222
	v_and_or_b32 v223, v178, 31, v130
	v_add_lshl_u32 v223, v223, v222, 1
	v_or_b32_e32 v205, 0x20000, v223
	v_lshrrev_b32_e32 v222, 2, v193
	v_and_or_b32 v222, v222, 8, v132
	v_mul_u32_u24_e32 v222, 0x110, v222
	v_and_or_b32 v223, v193, 31, v130
	v_add_lshl_u32 v223, v223, v222, 1
	v_or_b32_e32 v206, 0x20000, v223
	v_lshrrev_b32_e32 v222, 2, v192
	v_and_or_b32 v222, v222, 8, v132
	v_mul_u32_u24_e32 v222, 0x110, v222
	v_and_or_b32 v223, v192, 31, v130
	v_add_lshl_u32 v223, v223, v222, 1
	v_or_b32_e32 v207, 0x20000, v223
	s_movk_i32 s43, 0x110
	v_mad_u32_u24 v224, v179, s43, v203
	v_mov_b32_e32 v225, 0x20000
	v_lshl_or_b32 v224, v224, 1, v225
	s_lshl_b32 s43, s3, 1
	s_add_u32 s52, s43, 0
	s_and_b32 s52, s52, 7
	s_lshl_b32 s52, s52, 6
	s_nop 0
	v_add_u32_e32 v208, s52, v224
	s_add_u32 s52, s43, 1
	s_and_b32 s52, s52, 7
	s_lshl_b32 s52, s52, 6
	s_sub_u32 s52, s52, 64
	s_nop 0
	v_add_u32_e32 v209, s52, v224
	s_add_u32 s52, s43, 2
	s_and_b32 s52, s52, 7
	s_lshl_b32 s52, s52, 6
	s_nop 0
	v_add_u32_e32 v211, s52, v224
	s_add_u32 s52, s43, 3
	s_and_b32 s52, s52, 7
	s_lshl_b32 s52, s52, 6
	s_nop 0
	v_add_u32_e32 v212, s52, v224
	s_add_u32 s52, s43, 4
	s_and_b32 s52, s52, 7
	s_lshl_b32 s52, s52, 6
	s_nop 0
	v_add_u32_e32 v213, s52, v224
	s_add_u32 s52, s43, 5
	s_and_b32 s52, s52, 7
	s_lshl_b32 s52, s52, 6
	s_nop 0
	v_add_u32_e32 v214, s52, v224
	s_add_u32 s52, s43, 6
	s_and_b32 s52, s52, 7
	s_lshl_b32 s52, s52, 6
	s_nop 0
	v_add_u32_e32 v215, s52, v224
	s_add_u32 s52, s43, 7
	s_and_b32 s52, s52, 7
	s_lshl_b32 s52, s52, 6
	s_nop 0
	v_add_u32_e32 v216, s52, v224
	v_and_b32_e32 v225, 8, v0
	v_cmp_eq_u32_e32 vcc, 0, v225
	v_mov_b32_e32 v225, 0xeeeeeeee
	s_nop 1
	v_cndmask_b32_e32 v210, v225, v196, vcc
	v_and_b32_e32 v225, 47, v0
	v_cmp_eq_u32_e64 s[4:5], 0, v225
	v_lshlrev_b32_e32 v225, 4, v167
	v_lshlrev_b32_e32 v226, 3, v201
	s_mov_b32 s52, 0x24400
	v_or3_b32 v218, v225, v226, s52
	s_load_dwordx2 s[6:7], s[0:1], 0x18
	s_lshl_b32 s11, s2, 9
	s_mov_b64 s[22:23], 0
	s_mov_b32 s29, 0
	s_mov_b32 s30, 0
	v_mov_b32_e32 v221, 0
	s_mov_b32 s40, 0x3a000000
	s_mov_b32 s41, 0x34800000
	s_mov_b32 s42, 0x45000000
	v_mov_b32_e32 v217, 0x24480
	v_mov_b64_e32 v[230:231], 0
	v_mov_b64_e32 v[232:233], 0
	v_mov_b64_e32 v[234:235], 0
	v_mov_b64_e32 v[236:237], 0
	v_mov_b64_e32 v[238:239], 0
	v_mov_b64_e32 v[240:241], 0
	v_mov_b64_e32 v[242:243], 0
	v_mov_b64_e32 v[244:245], 0
	ds_write_b128 v217, v[230:233]
	v_mov_b32_e32 v178, 0
	v_fma_mixlo_f16 v131, v178, v238, v171
	v_fma_mixlo_f16 v139, v178, v238, v170
	v_fma_mixlo_f16 v147, v178, v238, v169
	v_fma_mixlo_f16 v155, v178, v238, v168
	v_fma_f32 v130, v178, v238, v171
	v_fma_f32 v138, v178, v238, v170
	v_fma_f32 v146, v178, v238, v169
	v_fma_f32 v154, v178, v238, v168
	v_fma_mix_f32 v130, v130, 1.0, -v131 op_sel_hi:[0,0,1]
	v_fma_mix_f32 v138, v138, 1.0, -v139 op_sel_hi:[0,0,1]
	v_fma_mix_f32 v146, v146, 1.0, -v147 op_sel_hi:[0,0,1]
	v_fma_mix_f32 v154, v154, 1.0, -v155 op_sel_hi:[0,0,1]
	v_fma_mixlo_f16 v133, v130, s42, 0
	v_fma_mixlo_f16 v141, v138, s42, 0
	v_fma_mixlo_f16 v149, v146, s42, 0
	v_fma_mixlo_f16 v157, v154, s42, 0
	v_fma_mix_f32 v130, v130, s42, -v133 op_sel_hi:[0,0,1]
	v_fma_mix_f32 v138, v138, s42, -v141 op_sel_hi:[0,0,1]
	v_fma_mix_f32 v146, v146, s42, -v149 op_sel_hi:[0,0,1]
	v_fma_mix_f32 v154, v154, s42, -v157 op_sel_hi:[0,0,1]
	v_fma_mixlo_f16 v132, v130, s42, 0
	v_fma_mixlo_f16 v140, v138, s42, 0
	v_fma_mixlo_f16 v148, v146, s42, 0
	v_fma_mixlo_f16 v156, v154, s42, 0
	ds_write_b16 v204, v131
	ds_write_b16 v205, v139
	ds_write_b16 v206, v147
	ds_write_b16 v207, v155
	ds_write_b16 v204, v133 offset:544
	ds_write_b16 v205, v141 offset:544
	ds_write_b16 v206, v149 offset:544
	ds_write_b16 v207, v157 offset:544
	ds_write_b16 v204, v132 offset:1088
	ds_write_b16 v205, v140 offset:1088
	ds_write_b16 v206, v148 offset:1088
	ds_write_b16 v207, v156 offset:1088
	ds_read_b128 v[180:183], v199 offset:0
	s_waitcnt lgkmcnt(6)
	ds_read_b128 v[184:187], v199 offset:1024
	ds_read_b128 v[188:191], v199 offset:4096
	ds_read_b128 v[192:195], v199 offset:5120
	ds_read_b128 v[222:225], v199 offset:8192
	ds_read_b128 v[226:229], v199 offset:9216
	s_mov_b32 s52, 0x3a83126f
	v_mov_b32_e32 v248, 0x358637bd
	s_waitcnt lgkmcnt(0)
	s_barrier
	ds_read_b128 v[130:133], v208
	ds_read_b128 v[134:137], v209 offset:64
	ds_read_b128 v[138:141], v211
	ds_read_b128 v[142:145], v212
	ds_read_b128 v[146:149], v213
	ds_read_b128 v[150:153], v214
	ds_read_b128 v[154:157], v215
	ds_read_b128 v[158:161], v216
	s_waitcnt lgkmcnt(7)
	v_smfmac_f32_16x16x64_f16 v[230:233], v[130:133], a[16:23], v210
	v_fma_f32 v179, |v171|, s52, v248
	v_fma_f32 v196, |v170|, s52, v248
	v_smfmac_f32_16x16x64_f16 v[234:237], v[130:133], v[180:187], v210
	ds_read_b128 v[180:183], v199 offset:12288
	ds_read_b128 v[184:187], v199 offset:13312
	v_fma_f32 v197, |v169|, s52, v248
	s_waitcnt lgkmcnt(8)
	v_smfmac_f32_16x16x64_f16 v[230:233], v[134:137], a[48:55], v210
	v_fma_f32 v198, |v168|, s52, v248
	v_smfmac_f32_16x16x64_f16 v[234:237], v[134:137], v[188:195], v210
	ds_read_b128 v[188:191], v199 offset:16384
	ds_read_b128 v[192:195], v199 offset:17408
	v_rcp_f32_e32 v179, v179
	s_waitcnt lgkmcnt(9)
	v_smfmac_f32_16x16x64_f16 v[230:233], v[138:141], a[80:87], v210
	v_rcp_f32_e32 v196, v196
	v_smfmac_f32_16x16x64_f16 v[234:237], v[138:141], v[222:229], v210
	ds_read_b128 v[222:225], v199 offset:20480
	ds_read_b128 v[226:229], v199 offset:21504
	v_rcp_f32_e32 v197, v197
	s_waitcnt lgkmcnt(10)
	v_smfmac_f32_16x16x64_f16 v[230:233], v[142:145], a[112:119], v210
	v_rcp_f32_e32 v198, v198
	s_waitcnt lgkmcnt(4)
	v_smfmac_f32_16x16x64_f16 v[234:237], v[142:145], v[180:187], v210
	ds_read_b128 v[180:183], v199 offset:24576
	ds_read_b128 v[184:187], v199 offset:25600
	v_mul_f32_e32 v249, v170, v196
	v_smfmac_f32_16x16x64_f16 v[230:233], v[146:149], a[144:151], v210
	v_mul_f32_e32 v166, v249, v249
	s_waitcnt lgkmcnt(4)
	v_smfmac_f32_16x16x64_f16 v[234:237], v[146:149], v[188:195], v210
	ds_read_b128 v[188:191], v199 offset:28672
	ds_read_b128 v[192:195], v199 offset:29696
	v_mul_f32_e32 v249, v171, v179
	v_smfmac_f32_16x16x64_f16 v[230:233], v[150:153], a[176:183], v210
	v_fmac_f32_e32 v166, v249, v249
	s_waitcnt lgkmcnt(4)
	v_smfmac_f32_16x16x64_f16 v[234:237], v[150:153], v[222:229], v210
	ds_read_b128 v[222:225], v199 offset:2048
	ds_read_b128 v[226:229], v199 offset:3072
	v_mul_f32_e32 v249, v169, v197
	v_smfmac_f32_16x16x64_f16 v[230:233], v[154:157], a[208:215], v210
	v_fmac_f32_e32 v166, v249, v249
	s_waitcnt lgkmcnt(4)
	v_smfmac_f32_16x16x64_f16 v[234:237], v[154:157], v[180:187], v210
	ds_read_b128 v[180:183], v199 offset:6144
	ds_read_b128 v[184:187], v199 offset:7168
	v_mul_f32_e32 v249, v168, v198
	s_waitcnt vmcnt(0)
	s_bfe_u32 s60, s2, 0x30003
	s_lshl_b32 s60, s60, 15
	v_lshl_add_u32 v251, v0, 7, s60
	global_load_dword v251, v251, s[12:13]
	v_smfmac_f32_16x16x64_f16 v[230:233], v[158:161], a[240:247], v210
	v_fmac_f32_e32 v166, v249, v249
	s_waitcnt lgkmcnt(4)
	v_smfmac_f32_16x16x64_f16 v[234:237], v[158:161], v[188:195], v210
	ds_read_b128 v[188:191], v199 offset:10240
	ds_read_b128 v[192:195], v199 offset:11264
	v_smfmac_f32_16x16x64_f16 v[238:241], v[130:133], a[24:31], v210
	s_waitcnt lgkmcnt(4)
	v_smfmac_f32_16x16x64_f16 v[242:245], v[130:133], v[222:229], v210
	ds_read_b128 v[222:225], v199 offset:14336
	ds_read_b128 v[226:229], v199 offset:15360
	v_smfmac_f32_16x16x64_f16 v[238:241], v[134:137], a[56:63], v210
	v_fmac_f32_e32 v230, s40, v231
	s_waitcnt lgkmcnt(4)
	v_smfmac_f32_16x16x64_f16 v[242:245], v[134:137], v[180:187], v210
	ds_read_b128 v[180:183], v199 offset:18432
	ds_read_b128 v[184:187], v199 offset:19456
	v_fmac_f32_e32 v234, s40, v235
	v_smfmac_f32_16x16x64_f16 v[238:241], v[138:141], a[88:95], v210
	v_fmac_f32_e32 v230, s41, v232
	s_waitcnt lgkmcnt(4)
	v_smfmac_f32_16x16x64_f16 v[242:245], v[138:141], v[188:195], v210
	ds_read_b128 v[188:191], v199 offset:22528
	ds_read_b128 v[192:195], v199 offset:23552
	v_fmac_f32_e32 v234, s41, v236
	v_smfmac_f32_16x16x64_f16 v[238:241], v[142:145], a[120:127], v210
	s_nop 0
	v_permlane32_swap_b32_e32 v230, v234
	s_waitcnt lgkmcnt(4)
	v_smfmac_f32_16x16x64_f16 v[242:245], v[142:145], v[222:229], v210
	ds_read_b128 v[222:225], v199 offset:26624
	ds_read_b128 v[226:229], v199 offset:27648
	v_add_f32_e32 v175, v230, v234
	v_smfmac_f32_16x16x64_f16 v[238:241], v[146:149], a[152:159], v210
	ds_read_b128 v[230:233], v217
	s_waitcnt lgkmcnt(5)
	v_smfmac_f32_16x16x64_f16 v[242:245], v[146:149], v[180:187], v210
	ds_read_b128 v[180:183], v199 offset:30720
	ds_read_b128 v[184:187], v199 offset:31744
	ds_read_b128 v[234:237], v217
	v_smfmac_f32_16x16x64_f16 v[238:241], v[150:153], a[184:191], v210
	s_waitcnt lgkmcnt(6)
	v_smfmac_f32_16x16x64_f16 v[242:245], v[150:153], v[188:195], v210
	v_smfmac_f32_16x16x64_f16 v[238:241], v[154:157], a[216:223], v210
	s_waitcnt lgkmcnt(4)
	v_smfmac_f32_16x16x64_f16 v[242:245], v[154:157], v[222:229], v210
	v_smfmac_f32_16x16x64_f16 v[238:241], v[158:161], a[248:255], v210
	s_waitcnt lgkmcnt(1)
	v_smfmac_f32_16x16x64_f16 v[242:245], v[158:161], v[180:187], v210
	v_smfmac_f32_16x16x64_f16 v[230:233], v[130:133], a[0:7], v210
	s_waitcnt lgkmcnt(0)
	v_smfmac_f32_16x16x64_f16 v[234:237], v[130:133], v[18:25], v210
	v_smfmac_f32_16x16x64_f16 v[230:233], v[134:137], a[40:47], v210
	v_fmac_f32_e32 v238, s40, v239
	v_smfmac_f32_16x16x64_f16 v[234:237], v[134:137], v[34:41], v210
	v_fmac_f32_e32 v242, s40, v243
	v_smfmac_f32_16x16x64_f16 v[230:233], v[138:141], a[64:71], v210
	v_fmac_f32_e32 v238, s41, v240
	v_smfmac_f32_16x16x64_f16 v[234:237], v[138:141], v[42:49], v210
	v_fmac_f32_e32 v242, s41, v244
	v_smfmac_f32_16x16x64_f16 v[230:233], v[142:145], a[96:103], v210
	s_nop 0
	v_permlane32_swap_b32_e32 v238, v242
	v_smfmac_f32_16x16x64_f16 v[234:237], v[142:145], v[58:65], v210
	v_add_f32_e32 v174, v238, v242
	v_smfmac_f32_16x16x64_f16 v[230:233], v[146:149], a[128:135], v210
	ds_read_b128 v[238:241], v217
	v_smfmac_f32_16x16x64_f16 v[234:237], v[146:149], v[74:81], v210
	ds_read_b128 v[242:245], v217
	v_smfmac_f32_16x16x64_f16 v[230:233], v[150:153], a[160:167], v210
	v_smfmac_f32_16x16x64_f16 v[234:237], v[150:153], v[98:105], v210
	v_smfmac_f32_16x16x64_f16 v[230:233], v[154:157], a[192:199], v210
	v_smfmac_f32_16x16x64_f16 v[234:237], v[154:157], v[106:113], v210
	v_smfmac_f32_16x16x64_f16 v[230:233], v[158:161], a[224:231], v210
	v_smfmac_f32_16x16x64_f16 v[234:237], v[158:161], v[122:129], v210
	s_waitcnt lgkmcnt(1)
	v_smfmac_f32_16x16x64_f16 v[238:241], v[130:133], a[8:15], v210
	s_waitcnt lgkmcnt(0)
	v_smfmac_f32_16x16x64_f16 v[242:245], v[130:133], v[2:9], v210
	v_smfmac_f32_16x16x64_f16 v[238:241], v[134:137], a[32:39], v210
	v_fmac_f32_e32 v230, s40, v231
	v_smfmac_f32_16x16x64_f16 v[242:245], v[134:137], v[10:17], v210
	v_fmac_f32_e32 v234, s40, v235
	v_smfmac_f32_16x16x64_f16 v[238:241], v[138:141], a[72:79], v210
	v_fmac_f32_e32 v230, s41, v232
	v_smfmac_f32_16x16x64_f16 v[242:245], v[138:141], v[50:57], v210
	v_fmac_f32_e32 v234, s41, v236
	v_smfmac_f32_16x16x64_f16 v[238:241], v[142:145], a[104:111], v210
	s_nop 0
	v_permlane32_swap_b32_e32 v230, v234
	v_smfmac_f32_16x16x64_f16 v[242:245], v[142:145], v[26:33], v210
	v_add_f32_e32 v173, v230, v234
	v_smfmac_f32_16x16x64_f16 v[238:241], v[146:149], a[136:143], v210
	ds_read_b128 v[230:233], v217
	v_smfmac_f32_16x16x64_f16 v[242:245], v[146:149], v[82:89], v210
	ds_read_b128 v[234:237], v217
	v_smfmac_f32_16x16x64_f16 v[238:241], v[150:153], a[168:175], v210
	v_smfmac_f32_16x16x64_f16 v[242:245], v[150:153], v[66:73], v210
	v_smfmac_f32_16x16x64_f16 v[238:241], v[154:157], a[200:207], v210
	v_smfmac_f32_16x16x64_f16 v[242:245], v[154:157], v[114:121], v210
	v_smfmac_f32_16x16x64_f16 v[238:241], v[158:161], a[232:239], v210
	v_smfmac_f32_16x16x64_f16 v[242:245], v[158:161], v[90:97], v210
	s_nop 6
	v_fmac_f32_e32 v238, s40, v239
	v_fmac_f32_e32 v242, s40, v243
	v_fmac_f32_e32 v238, s41, v240
	v_fmac_f32_e32 v242, s41, v244
	s_nop 1
	v_permlane32_swap_b32_e32 v238, v242
	v_add_f32_e32 v172, v238, v242
	ds_read_b128 v[180:183], v199 offset:0
	ds_read_b128 v[184:187], v199 offset:1024
	ds_read_b128 v[188:191], v199 offset:4096
	ds_read_b128 v[192:195], v199 offset:5120
	ds_read_b128 v[222:225], v199 offset:8192
	ds_read_b128 v[226:229], v199 offset:9216
	v_mul_f32_e32 v239, 0x3b000000, v172
	v_mul_f32_e32 v239, v239, v196
	v_mul_f32_e32 v167, v239, v239
	v_mul_f32_e32 v239, 0x3b000000, v173
	v_mul_f32_e32 v239, v239, v179
	v_fmac_f32_e32 v167, v239, v239
	v_mul_f32_e32 v239, 0x3b000000, v175
	v_mul_f32_e32 v239, v239, v197
	v_fmac_f32_e32 v167, v239, v239
	v_mul_f32_e32 v239, 0x3b000000, v174
	v_mul_f32_e32 v239, v239, v198
	v_fmac_f32_e32 v167, v239, v239
	v_mov_b32_e32 v130, v166
	v_mov_b32_e32 v131, v167
	s_nop 0
	v_add_f32_dpp v130, v130, v130 quad_perm:[1,0,3,2] row_mask:0xf bank_mask:0xf bound_ctrl:1
	v_add_f32_dpp v131, v131, v131 quad_perm:[1,0,3,2] row_mask:0xf bank_mask:0xf bound_ctrl:1
	s_nop 0
	v_add_f32_dpp v130, v130, v130 quad_perm:[2,3,0,1] row_mask:0xf bank_mask:0xf bound_ctrl:1
	v_add_f32_dpp v131, v131, v131 quad_perm:[2,3,0,1] row_mask:0xf bank_mask:0xf bound_ctrl:1
	s_nop 0
	v_add_f32_dpp v130, v130, v130 row_half_mirror row_mask:0xf bank_mask:0xf bound_ctrl:1
	v_add_f32_dpp v131, v131, v131 row_half_mirror row_mask:0xf bank_mask:0xf bound_ctrl:1
	s_nop 0
	v_add_f32_dpp v130, v130, v130 row_mirror row_mask:0xf bank_mask:0xf bound_ctrl:1
	v_add_f32_dpp v131, v131, v131 row_mirror row_mask:0xf bank_mask:0xf bound_ctrl:1
	v_mov_b32_e32 v240, v130
	v_mov_b32_e32 v241, v131
	s_nop 0
	v_permlane32_swap_b32_e32 v130, v240
	v_permlane32_swap_b32_e32 v131, v241
	v_add_f32_e32 v130, v130, v240
	v_add_f32_e32 v131, v131, v241
	v_add_u32_e32 v242, 0, v218
	v_lshlrev_b32_e32 v243, 3, v201
	v_or_b32_e32 v243, 0x24400, v243
	s_and_saveexec_b64 s[2:3], s[4:5]
	ds_write_b64 v242, v[130:131]
	s_or_b64 exec, exec, s[2:3]
	s_waitcnt lgkmcnt(0)
	s_barrier
	ds_read_b64 v[134:135], v243 offset:0
	ds_read_b64 v[138:139], v243 offset:16
	ds_read_b64 v[142:143], v243 offset:32
	ds_read_b64 v[146:147], v243 offset:48
	s_waitcnt lgkmcnt(2)
	v_add_f32_e32 v238, v134, v138
	s_waitcnt lgkmcnt(1)
	v_add_f32_e32 v238, v238, v142
	s_waitcnt lgkmcnt(0)
	v_add_f32_e32 v238, v238, v146
	v_add_f32_e32 v239, v135, v139
	v_add_f32_e32 v239, v239, v143
	v_add_f32_e32 v239, v239, v147
	v_mul_f32_e32 v238, 0x3b000000, v238
	v_max_f32_e32 v238, 0xda24260, v238
	v_sqrt_f32_e32 v238, v238
	v_mul_f32_e32 v239, 0x3b000000, v239
	v_max_f32_e32 v239, 0xda24260, v239
	v_sqrt_f32_e32 v239, v239
	s_nop 0
	v_mov_b32_e32 v220, v239
	v_rcp_f32_e32 v240, v239
	v_min_f32_e32 v241, v238, v239
	v_mul_f32_e32 v238, 0x3c23d70a, v238
	v_mul_f32_e32 v238, v238, v240
	s_mov_b32 s52, 0x3727c5ac
	v_cmp_ngt_f32_e32 vcc, s52, v241
	v_mov_b32_e32 v240, 0x358637bd
	s_nop 1
	v_cndmask_b32_e32 v219, v240, v238, vcc
	v_mul_f32_e32 v178, 0x3b000000, v219
	v_fma_mixlo_f16 v131, v178, v173, v171
	v_fma_mixlo_f16 v139, v178, v172, v170
	v_fma_mixlo_f16 v147, v178, v175, v169
	v_fma_mixlo_f16 v155, v178, v174, v168
	v_fma_f32 v130, v178, v173, v171
	v_fma_f32 v138, v178, v172, v170
	v_fma_f32 v146, v178, v175, v169
	v_fma_f32 v154, v178, v174, v168
	v_fma_mix_f32 v130, v130, 1.0, -v131 op_sel_hi:[0,0,1]
	v_fma_mix_f32 v138, v138, 1.0, -v139 op_sel_hi:[0,0,1]
	v_fma_mix_f32 v146, v146, 1.0, -v147 op_sel_hi:[0,0,1]
	v_fma_mix_f32 v154, v154, 1.0, -v155 op_sel_hi:[0,0,1]
	v_fma_mixlo_f16 v133, v130, s42, 0
	v_fma_mixlo_f16 v141, v138, s42, 0
	v_fma_mixlo_f16 v149, v146, s42, 0
	v_fma_mixlo_f16 v157, v154, s42, 0
	v_fma_mix_f32 v130, v130, s42, -v133 op_sel_hi:[0,0,1]
	v_fma_mix_f32 v138, v138, s42, -v141 op_sel_hi:[0,0,1]
	v_fma_mix_f32 v146, v146, s42, -v149 op_sel_hi:[0,0,1]
	v_fma_mix_f32 v154, v154, s42, -v157 op_sel_hi:[0,0,1]
	v_fma_mixlo_f16 v132, v130, s42, 0
	v_fma_mixlo_f16 v140, v138, s42, 0
	v_fma_mixlo_f16 v148, v146, s42, 0
	v_fma_mixlo_f16 v156, v154, s42, 0
	ds_write_b16 v204, v131 offset:8704
	ds_write_b16 v205, v139 offset:8704
	ds_write_b16 v206, v147 offset:8704
	ds_write_b16 v207, v155 offset:8704
	ds_write_b16 v204, v133 offset:9248
	ds_write_b16 v205, v141 offset:9248
	ds_write_b16 v206, v149 offset:9248
	ds_write_b16 v207, v157 offset:9248
	ds_write_b16 v204, v132 offset:9792
	ds_write_b16 v205, v140 offset:9792
	ds_write_b16 v206, v148 offset:9792
	ds_write_b16 v207, v156 offset:9792
	s_waitcnt lgkmcnt(0)
	s_barrier
	ds_read_b128 v[130:133], v208 offset:8704
	ds_read_b128 v[134:137], v209 offset:8768
	ds_read_b128 v[138:141], v211 offset:8704
	ds_read_b128 v[142:145], v212 offset:8704
	ds_read_b128 v[146:149], v213 offset:8704
	ds_read_b128 v[150:153], v214 offset:8704
	ds_read_b128 v[154:157], v215 offset:8704
	ds_read_b128 v[158:161], v216 offset:8704
	s_waitcnt lgkmcnt(7)
	v_smfmac_f32_16x16x64_f16 v[230:233], v[130:133], a[16:23], v210
	ds_read_b128 v[238:241], v217
	v_smfmac_f32_16x16x64_f16 v[234:237], v[130:133], v[180:187], v210
	ds_read_b128 v[180:183], v199 offset:12288
	ds_read_b128 v[184:187], v199 offset:13312
	ds_read_b128 v[242:245], v217
	s_waitcnt lgkmcnt(10)
	v_smfmac_f32_16x16x64_f16 v[230:233], v[134:137], a[48:55], v210
	v_smfmac_f32_16x16x64_f16 v[234:237], v[134:137], v[188:195], v210
	ds_read_b128 v[188:191], v199 offset:16384
	ds_read_b128 v[192:195], v199 offset:17408
	s_waitcnt lgkmcnt(11)
	v_smfmac_f32_16x16x64_f16 v[230:233], v[138:141], a[80:87], v210
	v_smfmac_f32_16x16x64_f16 v[234:237], v[138:141], v[222:229], v210
	ds_read_b128 v[222:225], v199 offset:20480
	ds_read_b128 v[226:229], v199 offset:21504
	s_waitcnt lgkmcnt(12)
	v_smfmac_f32_16x16x64_f16 v[230:233], v[142:145], a[112:119], v210
	s_waitcnt lgkmcnt(5)
	v_smfmac_f32_16x16x64_f16 v[234:237], v[142:145], v[180:187], v210
	ds_read_b128 v[180:183], v199 offset:24576
	ds_read_b128 v[184:187], v199 offset:25600
	v_smfmac_f32_16x16x64_f16 v[230:233], v[146:149], a[144:151], v210
	s_waitcnt lgkmcnt(4)
	v_smfmac_f32_16x16x64_f16 v[234:237], v[146:149], v[188:195], v210
	ds_read_b128 v[188:191], v199 offset:28672
	ds_read_b128 v[192:195], v199 offset:29696
	v_smfmac_f32_16x16x64_f16 v[230:233], v[150:153], a[176:183], v210
	s_waitcnt lgkmcnt(4)
	v_smfmac_f32_16x16x64_f16 v[234:237], v[150:153], v[222:229], v210
	ds_read_b128 v[222:225], v199 offset:2048
	ds_read_b128 v[226:229], v199 offset:3072
	v_smfmac_f32_16x16x64_f16 v[230:233], v[154:157], a[208:215], v210
	s_waitcnt lgkmcnt(4)
	v_smfmac_f32_16x16x64_f16 v[234:237], v[154:157], v[180:187], v210
	ds_read_b128 v[180:183], v199 offset:6144
	ds_read_b128 v[184:187], v199 offset:7168
	v_smfmac_f32_16x16x64_f16 v[230:233], v[158:161], a[240:247], v210
	s_waitcnt lgkmcnt(4)
	v_smfmac_f32_16x16x64_f16 v[234:237], v[158:161], v[188:195], v210
	ds_read_b128 v[188:191], v199 offset:10240
	ds_read_b128 v[192:195], v199 offset:11264
	v_smfmac_f32_16x16x64_f16 v[238:241], v[130:133], a[24:31], v210
	s_waitcnt lgkmcnt(4)
	v_smfmac_f32_16x16x64_f16 v[242:245], v[130:133], v[222:229], v210
	ds_read_b128 v[222:225], v199 offset:14336
	ds_read_b128 v[226:229], v199 offset:15360
	v_smfmac_f32_16x16x64_f16 v[238:241], v[134:137], a[56:63], v210
	v_fmac_f32_e32 v230, s40, v231
	s_waitcnt lgkmcnt(4)
	v_smfmac_f32_16x16x64_f16 v[242:245], v[134:137], v[180:187], v210
	ds_read_b128 v[180:183], v199 offset:18432
	ds_read_b128 v[184:187], v199 offset:19456
	v_fmac_f32_e32 v234, s40, v235
	v_smfmac_f32_16x16x64_f16 v[238:241], v[138:141], a[88:95], v210
	v_fmac_f32_e32 v230, s41, v232
	s_waitcnt lgkmcnt(4)
	v_smfmac_f32_16x16x64_f16 v[242:245], v[138:141], v[188:195], v210
	ds_read_b128 v[188:191], v199 offset:22528
	ds_read_b128 v[192:195], v199 offset:23552
	v_fmac_f32_e32 v234, s41, v236
	v_smfmac_f32_16x16x64_f16 v[238:241], v[142:145], a[120:127], v210
	s_nop 0
	v_permlane32_swap_b32_e32 v230, v234
	s_waitcnt lgkmcnt(4)
	v_smfmac_f32_16x16x64_f16 v[242:245], v[142:145], v[222:229], v210
	ds_read_b128 v[222:225], v199 offset:26624
	ds_read_b128 v[226:229], v199 offset:27648
	v_add_f32_e32 v164, v230, v234
	v_smfmac_f32_16x16x64_f16 v[238:241], v[146:149], a[152:159], v210
	ds_read_b128 v[230:233], v217
	s_waitcnt lgkmcnt(5)
	v_smfmac_f32_16x16x64_f16 v[242:245], v[146:149], v[180:187], v210
	ds_read_b128 v[180:183], v199 offset:30720
	ds_read_b128 v[184:187], v199 offset:31744
	ds_read_b128 v[234:237], v217
	v_smfmac_f32_16x16x64_f16 v[238:241], v[150:153], a[184:191], v210
	s_waitcnt lgkmcnt(6)
	v_smfmac_f32_16x16x64_f16 v[242:245], v[150:153], v[188:195], v210
	v_smfmac_f32_16x16x64_f16 v[238:241], v[154:157], a[216:223], v210
	s_waitcnt lgkmcnt(4)
	v_smfmac_f32_16x16x64_f16 v[242:245], v[154:157], v[222:229], v210
	v_smfmac_f32_16x16x64_f16 v[238:241], v[158:161], a[248:255], v210
	s_waitcnt lgkmcnt(1)
	v_smfmac_f32_16x16x64_f16 v[242:245], v[158:161], v[180:187], v210
	v_smfmac_f32_16x16x64_f16 v[230:233], v[130:133], a[0:7], v210
	s_waitcnt lgkmcnt(0)
	v_smfmac_f32_16x16x64_f16 v[234:237], v[130:133], v[18:25], v210
	v_smfmac_f32_16x16x64_f16 v[230:233], v[134:137], a[40:47], v210
	v_fmac_f32_e32 v238, s40, v239
	v_smfmac_f32_16x16x64_f16 v[234:237], v[134:137], v[34:41], v210
	v_fmac_f32_e32 v242, s40, v243
	v_smfmac_f32_16x16x64_f16 v[230:233], v[138:141], a[64:71], v210
	v_fmac_f32_e32 v238, s41, v240
	v_smfmac_f32_16x16x64_f16 v[234:237], v[138:141], v[42:49], v210
	v_fmac_f32_e32 v242, s41, v244
	v_smfmac_f32_16x16x64_f16 v[230:233], v[142:145], a[96:103], v210
	s_nop 0
	v_permlane32_swap_b32_e32 v238, v242
	v_smfmac_f32_16x16x64_f16 v[234:237], v[142:145], v[58:65], v210
	v_add_f32_e32 v165, v238, v242
	v_smfmac_f32_16x16x64_f16 v[230:233], v[146:149], a[128:135], v210
	ds_read_b128 v[238:241], v217
	v_smfmac_f32_16x16x64_f16 v[234:237], v[146:149], v[74:81], v210
	ds_read_b128 v[242:245], v217
	v_smfmac_f32_16x16x64_f16 v[230:233], v[150:153], a[160:167], v210
	v_smfmac_f32_16x16x64_f16 v[234:237], v[150:153], v[98:105], v210
	v_smfmac_f32_16x16x64_f16 v[230:233], v[154:157], a[192:199], v210
	v_smfmac_f32_16x16x64_f16 v[234:237], v[154:157], v[106:113], v210
	v_smfmac_f32_16x16x64_f16 v[230:233], v[158:161], a[224:231], v210
	v_smfmac_f32_16x16x64_f16 v[234:237], v[158:161], v[122:129], v210
	s_waitcnt lgkmcnt(1)
	v_smfmac_f32_16x16x64_f16 v[238:241], v[130:133], a[8:15], v210
	s_waitcnt lgkmcnt(0)
	v_smfmac_f32_16x16x64_f16 v[242:245], v[130:133], v[2:9], v210
	v_smfmac_f32_16x16x64_f16 v[238:241], v[134:137], a[32:39], v210
	v_fmac_f32_e32 v230, s40, v231
	v_smfmac_f32_16x16x64_f16 v[242:245], v[134:137], v[10:17], v210
	v_fmac_f32_e32 v234, s40, v235
	v_smfmac_f32_16x16x64_f16 v[238:241], v[138:141], a[72:79], v210
	v_fmac_f32_e32 v230, s41, v232
	v_smfmac_f32_16x16x64_f16 v[242:245], v[138:141], v[50:57], v210
	v_fmac_f32_e32 v234, s41, v236
	v_smfmac_f32_16x16x64_f16 v[238:241], v[142:145], a[104:111], v210
	s_nop 0
	v_permlane32_swap_b32_e32 v230, v234
	v_smfmac_f32_16x16x64_f16 v[242:245], v[142:145], v[26:33], v210
	v_add_f32_e32 v162, v230, v234
	v_smfmac_f32_16x16x64_f16 v[238:241], v[146:149], a[136:143], v210
	ds_read_b128 v[230:233], v217
	v_smfmac_f32_16x16x64_f16 v[242:245], v[146:149], v[82:89], v210
	ds_read_b128 v[234:237], v217
	v_smfmac_f32_16x16x64_f16 v[238:241], v[150:153], a[168:175], v210
	v_smfmac_f32_16x16x64_f16 v[242:245], v[150:153], v[66:73], v210
	v_smfmac_f32_16x16x64_f16 v[238:241], v[154:157], a[200:207], v210
	v_smfmac_f32_16x16x64_f16 v[242:245], v[154:157], v[114:121], v210
	v_smfmac_f32_16x16x64_f16 v[238:241], v[158:161], a[232:239], v210
	v_smfmac_f32_16x16x64_f16 v[242:245], v[158:161], v[90:97], v210
	s_nop 6
	v_fmac_f32_e32 v238, s40, v239
	v_fmac_f32_e32 v242, s40, v243
	v_fmac_f32_e32 v238, s41, v240
	v_fmac_f32_e32 v242, s41, v244
	s_nop 1
	v_permlane32_swap_b32_e32 v238, v242
	v_add_f32_e32 v163, v238, v242
	ds_read_b128 v[180:183], v199 offset:0
	ds_read_b128 v[184:187], v199 offset:1024
	ds_read_b128 v[188:191], v199 offset:4096
	ds_read_b128 v[192:195], v199 offset:5120
	ds_read_b128 v[222:225], v199 offset:8192
	ds_read_b128 v[226:229], v199 offset:9216
	v_sub_f32_e32 v238, v163, v172
	v_mul_f32_e32 v238, 0x3b000000, v238
	v_mul_f32_e32 v238, v238, v196
	v_mul_f32_e32 v130, v238, v238
	v_sub_f32_e32 v238, v162, v173
	v_mul_f32_e32 v238, 0x3b000000, v238
	v_mul_f32_e32 v238, v238, v179
	v_fmac_f32_e32 v130, v238, v238
	v_sub_f32_e32 v238, v164, v175
	v_mul_f32_e32 v238, 0x3b000000, v238
	v_mul_f32_e32 v238, v238, v197
	v_fmac_f32_e32 v130, v238, v238
	v_sub_f32_e32 v238, v165, v174
	v_mul_f32_e32 v238, 0x3b000000, v238
	v_mul_f32_e32 v238, v238, v198
	v_fmac_f32_e32 v130, v238, v238
	s_nop 1
	v_add_f32_dpp v130, v130, v130 quad_perm:[1,0,3,2] row_mask:0xf bank_mask:0xf bound_ctrl:1
	s_nop 1
	v_add_f32_dpp v130, v130, v130 quad_perm:[2,3,0,1] row_mask:0xf bank_mask:0xf bound_ctrl:1
	s_nop 1
	v_add_f32_dpp v130, v130, v130 row_half_mirror row_mask:0xf bank_mask:0xf bound_ctrl:1
	s_nop 1
	v_add_f32_dpp v130, v130, v130 row_mirror row_mask:0xf bank_mask:0xf bound_ctrl:1
	v_mov_b32_e32 v240, v130
	s_nop 1
	v_permlane32_swap_b32_e32 v130, v240
	v_add_f32_e32 v130, v130, v240
	v_add_u32_e32 v242, 64, v218
	v_lshlrev_b32_e32 v243, 3, v201
	v_or_b32_e32 v243, 0x24440, v243
	s_and_saveexec_b64 s[2:3], s[4:5]
	ds_write_b32 v242, v130
	s_or_b64 exec, exec, s[2:3]
	s_waitcnt lgkmcnt(0)
	s_barrier
	ds_read2_b32 v[134:135], v243 offset1:4
	ds_read2_b32 v[136:137], v243 offset0:8 offset1:12
	s_waitcnt lgkmcnt(1)
	v_add_f32_e32 v238, v134, v135
	s_waitcnt lgkmcnt(0)
	v_add_f32_e32 v238, v238, v136
	v_add_f32_e32 v238, v238, v137
	v_mul_f32_e32 v238, 0x3b000000, v238
	v_max_f32_e32 v238, 0xda24260, v238
	v_rcp_f32_e32 v240, v219
	v_sqrt_f32_e32 v238, v238
	s_nop 0
	v_mul_f32_e32 v238, v240, v238
	v_max_f32_e32 v241, v220, v238
	v_mul_f32_e32 v242, 0x3a83126f, v219
	v_max_f32_e32 v242, 0x358637bd, v242
	v_max_f32_e32 v243, 0x26901d7d, v241
	v_rcp_f32_e32 v243, v243
	s_nop 0
	v_mul_f32_e32 v243, 0x3c23d70a, v243
	v_log_f32_e32 v243, v243
	s_nop 0
	v_mul_f32_e32 v243, 0x3e4ccccd, v243
	v_exp_f32_e32 v243, v243
	s_mov_b32 s52, 0x26901d7d
	v_cmp_ge_f32_e32 vcc, s52, v241
	s_nop 1
	v_cndmask_b32_e32 v243, v243, v242, vcc
	v_mul_f32_e32 v242, 0x42c80000, v219
	v_min3_f32 v1, v242, v243, 1.0
	s_waitcnt vmcnt(0)
